# attention inst1 loop software-pipelined in each wave: QK of tile t+1 interleaved with softmax of tile t, K/V prefetched two tiles ahead (3 K / 4 V LDS slots), K swizzle fix
# speedup vs baseline: 1.0048x; 1.0032x over previous
.LBB0_799:
	s_mov_b64 s[0:1], s[54:55]
	s_load_dword s0, s[0:1], 0x138
	v_writelane_b32 v254, s54, 20
	s_waitcnt lgkmcnt(0)
	s_cmp_gt_i32 s0, 4
	v_writelane_b32 v254, s55, 21
	v_writelane_b32 v254, s57, 22
	v_writelane_b32 v254, s56, 23
	s_cbranch_scc1 .LBB0_1087
	s_mov_b64 s[0:1], s[54:55]
	s_load_dword s0, s[0:1], 0x13c
	s_waitcnt lgkmcnt(0)
	s_cmp_lt_i32 s0, 5
	s_cbranch_scc1 .LBB0_1087
	s_mov_b64 s[0:1], s[54:55]
	v_mov_b32_e32 v1, v0
	s_andn2_b64 vcc, exec, s[12:13]
	v_readfirstlane_b32 s10, v1
	s_cbranch_vccnz .LBB0_1087
	s_load_dwordx2 s[2:3], s[0:1], 0x130
	s_load_dwordx2 s[4:5], s[0:1], 0x48
	s_waitcnt vmcnt(0)
	v_mbcnt_lo_u32_b32 v2, -1, 0
	s_mov_b32 s13, 0
	s_movk_i32 s68, 0xc00
	s_waitcnt lgkmcnt(0)
	s_add_u32 s6, s2, 0x1d000000
	s_addc_u32 s7, s3, 0
	s_add_u32 s33, s2, 0x23000000
	s_addc_u32 s58, s3, 0
	s_add_u32 s59, s2, 0x29000000
	s_addc_u32 s60, s3, 0
	s_add_u32 s61, s2, 0x4000000
	s_addc_u32 s62, s3, 0
	s_ashr_i32 s0, s10, 6
	s_add_u32 s10, s2, 0x32e0000
	s_addc_u32 s11, s3, 0
	s_lshl_b32 s63, s0, 5
	s_lshl_b32 s1, s0, 8
	s_lshl_b32 s0, s0, 10
	s_add_i32 s64, s0, 0
	s_add_i32 s65, s1, 0
	s_add_i32 s65, s65, 0x22000
	s_lshl_b32 s66, s93, 1
	s_lshl_b32 s67, s92, 1
	v_mov_b64_e32 v[146:147], s[6:7]
	v_mov_b32_e32 v162, 0xc00
	v_mov_b32_e32 v149, 0
	v_mov_b32_e32 v163, 0x358637bd
	s_mov_b32 s69, 0x800000
	s_mov_b32 s70, 0x2aaaaaab
	s_add_i32 s71, s64, 0x8000
	s_add_i32 s72, s64, 0xa000
	s_add_i32 s73, s64, 0xc000
	s_add_i32 s74, s64, 0x2000
	s_movk_i32 s75, 0x118
	s_mov_b32 s76, 0x41380000
	s_mov_b64 s[14:15], 0x20000
	s_mov_b64 s[16:17], 0x30000
	v_mbcnt_hi_u32_b32 v164, -1, v2
	s_mov_b32 s77, 0xc3e00000
	s_mov_b64 s[18:19], 0x4000
	s_mov_b64 s[20:21], 0x4800
	s_mov_b64 s[22:23], 0x5000
	s_mov_b64 s[24:25], 0x5800
	s_mov_b64 s[26:27], 0x8000
	s_mov_b64 s[28:29], 0x8800
	s_mov_b64 s[30:31], 0x9000
	s_mov_b64 s[34:35], 0x9800
	s_mov_b64 s[36:37], 0xc000
	s_mov_b64 s[38:39], 0xc800
	s_mov_b64 s[40:41], 0xd000
	s_mov_b64 s[42:43], 0xd800
	v_mov_b32_e32 v165, 0xff800000
	v_mov_b32_e32 v166, 0x43e00000
	s_mov_b32 s78, s93
	s_branch .LBB0_804

.LBB0_804:
	s_bfe_u32 s0, s66, 0x20001
	s_bfe_u32 s1, s78, 0x10007
	s_lshl_b32 s12, s1, 8
	s_lshl_b32 s44, s0, 9
	s_or_b32 s48, s44, s12
	s_mulk_i32 s0, 0x180
	s_mul_i32 s12, s1, 0xc0
	s_add_i32 s0, s0, s12
	s_lshl_b32 s50, s0, 1
	s_ashr_i32 s0, s78, 4
	s_lshl_b32 s12, s78, 1
	s_and_b32 s0, s0, -16
	s_and_b32 s44, s12, 8
	s_bfe_u32 s80, s78, 0x40003
	s_or_b32 s0, s0, s44
	s_xor_b32 s49, s80, 31
	s_ashr_i32 s0, s0, 3
	s_and_b32 s12, s12, 6
	s_lshl_b32 s83, s49, 8
	s_or_b32 s46, s12, s1
	s_ashr_i32 s1, s0, 31
	s_add_i32 s84, s83, s63
	s_lshr_b32 s81, s78, 3
	v_mov_b32_e32 v172, v1
	s_lshl_b64 s[52:53], s[0:1], 13
	s_ashr_i32 s12, s84, 31
	s_add_u32 s54, s52, s84
	v_and_b32_e32 v168, 31, v172
	v_or_b32_e32 v38, s54, v168
	s_addc_u32 s55, s53, s12
	v_mad_u64_u32 v[2:3], s[44:45], v38, s68, v[146:147]
	s_mul_i32 s82, s46, 0xc0
	v_bfe_u32 v173, v172, 5, 1
	v_mad_i32_i24 v3, s55, v162, v3
	s_lshl_b32 s12, s82, 1
	v_lshl_add_u64 v[2:3], v[2:3], 0, s[12:13]
	v_lshlrev_b32_e32 v148, 4, v173
	v_lshl_add_u64 v[40:41], v[2:3], 0, v[148:149]
	global_load_dwordx4 v[6:9], v[40:41], off
	global_load_dwordx4 v[14:17], v[40:41], off offset:32
	global_load_dwordx4 v[30:33], v[40:41], off offset:64
	global_load_dwordx4 v[34:37], v[40:41], off offset:96
	global_load_dwordx4 v[50:53], v[40:41], off offset:128
	global_load_dwordx4 v[26:29], v[40:41], off offset:160
	global_load_dwordx4 v[22:25], v[40:41], off offset:192
	global_load_dwordx4 v[18:21], v[40:41], off offset:224
	global_load_dwordx4 v[10:13], v[40:41], off offset:256
	global_load_dwordx4 v[42:45], v[40:41], off offset:288
	s_waitcnt lgkmcnt(0)
	global_load_dwordx4 v[2:5], v[40:41], off offset:320
	global_load_dwordx4 v[46:49], v[40:41], off offset:352
	v_and_b32_e32 v40, 32, v172
	v_mov_b32_e32 v39, s55
	s_mul_i32 s86, s0, 0x1800000
	s_mul_hi_i32 s51, s0, 0x1800000
	s_add_u32 s44, s33, s86
	s_addc_u32 s45, s58, s51
	s_lshl_b64 s[56:57], s[0:1], 24
	s_lshl_b32 s79, s46, 7
	s_add_u32 s44, s44, s12
	s_addc_u32 s45, s45, 0
	s_mov_b32 m0, s71
	s_add_u32 s0, s59, s56
	s_addc_u32 s1, s60, s57
	s_lshl_b32 s12, s46, 8
	s_add_u32 s46, s0, s12
	s_addc_u32 s47, s1, 0
	s_lshl_b32 s85, s49, 2
	s_add_i32 s85, s85, 4
	s_or_b32 s48, s56, s48
	s_add_u32 s48, s48, 0x29020000
	s_addc_u32 s49, s57, 0
	s_or_b32 s50, s86, s50
	s_add_u32 s50, s50, 0x23030000
	s_addc_u32 s51, s51, 0
	s_mov_b32 s12, 1
	s_movk_i32 s86, 0xff00
	s_waitcnt vmcnt(0)
	v_lshlrev_b32_e32 v227, 16, v26
	v_lshlrev_b32_e32 v177, 16, v6
	v_and_b32_e32 v174, 0xffff0000, v6
	v_lshlrev_b32_e32 v170, 16, v7
	v_and_b32_e32 v167, 0xffff0000, v7
	v_lshlrev_b32_e32 v180, 16, v8
	v_and_b32_e32 v176, 0xffff0000, v8
	v_lshlrev_b32_e32 v171, 16, v9
	v_and_b32_e32 v169, 0xffff0000, v9
	v_lshlrev_b32_e32 v185, 16, v14
	v_and_b32_e32 v182, 0xffff0000, v14
	v_lshlrev_b32_e32 v179, 16, v15
	v_and_b32_e32 v175, 0xffff0000, v15
	v_lshlrev_b32_e32 v187, 16, v16
	v_and_b32_e32 v183, 0xffff0000, v16
	v_lshlrev_b32_e32 v181, 16, v17
	v_and_b32_e32 v178, 0xffff0000, v17
	v_lshlrev_b32_e32 v201, 16, v34
	v_and_b32_e32 v198, 0xffff0000, v34
	v_lshlrev_b32_e32 v196, 16, v35
	v_and_b32_e32 v192, 0xffff0000, v35
	v_lshlrev_b32_e32 v202, 16, v36
	v_and_b32_e32 v199, 0xffff0000, v36
	v_lshlrev_b32_e32 v197, 16, v37
	v_and_b32_e32 v194, 0xffff0000, v37
	v_and_b32_e32 v228, 0xffff0000, v26
	global_load_dwordx4 v[142:145], v40, s[4:5] offset:704
	global_load_dwordx4 v[130:133], v40, s[4:5] offset:720
	global_load_dwordx4 v[6:9], v40, s[4:5] offset:592
	v_lshlrev_b32_e32 v229, 16, v27
	global_load_dwordx4 v[14:17], v40, s[4:5] offset:576
	v_and_b32_e32 v230, 0xffff0000, v27
	v_lshlrev_b32_e32 v231, 16, v28
	v_and_b32_e32 v232, 0xffff0000, v28
	v_lshlrev_b32_e32 v233, 16, v29
	v_and_b32_e32 v234, 0xffff0000, v29
	global_load_dwordx4 v[34:37], v40, s[4:5] offset:640
	global_load_dwordx4 v[156:159], v40, s[4:5] offset:656
	global_load_dwordx4 v[26:29], v40, s[4:5] offset:528
	v_mul_f32_e32 v209, v174, v174
	v_fmac_f32_e32 v209, v177, v177
	v_fmac_f32_e32 v209, v170, v170
	v_fmac_f32_e32 v209, v167, v167
	v_fmac_f32_e32 v209, v180, v180
	v_fmac_f32_e32 v209, v176, v176
	v_fmac_f32_e32 v209, v171, v171
	v_fmac_f32_e32 v209, v169, v169
	v_fmac_f32_e32 v209, v185, v185
	v_lshlrev_b32_e32 v193, 16, v30
	v_and_b32_e32 v190, 0xffff0000, v30
	v_lshlrev_b32_e32 v188, 16, v31
	v_and_b32_e32 v184, 0xffff0000, v31
	v_lshlrev_b32_e32 v195, 16, v32
	v_and_b32_e32 v191, 0xffff0000, v32
	v_lshlrev_b32_e32 v189, 16, v33
	v_and_b32_e32 v186, 0xffff0000, v33
	v_fmac_f32_e32 v209, v182, v182
	global_load_dwordx4 v[30:33], v40, s[4:5] offset:512
	v_fmac_f32_e32 v209, v179, v179
	v_fmac_f32_e32 v209, v175, v175
	v_fmac_f32_e32 v209, v187, v187
	v_fmac_f32_e32 v209, v183, v183
	v_fmac_f32_e32 v209, v181, v181
	v_fmac_f32_e32 v209, v178, v178
	v_fmac_f32_e32 v209, v193, v193
	v_fmac_f32_e32 v209, v190, v190
	v_fmac_f32_e32 v209, v188, v188
	v_fmac_f32_e32 v209, v184, v184
	v_fmac_f32_e32 v209, v195, v195
	v_fmac_f32_e32 v209, v191, v191
	v_fmac_f32_e32 v209, v189, v189
	v_fmac_f32_e32 v209, v186, v186
	v_fmac_f32_e32 v209, v201, v201
	v_fmac_f32_e32 v209, v198, v198
	v_fmac_f32_e32 v209, v196, v196
	v_fmac_f32_e32 v209, v192, v192
	v_fmac_f32_e32 v209, v202, v202
	v_fmac_f32_e32 v209, v199, v199
	v_fmac_f32_e32 v209, v197, v197
	v_lshlrev_b32_e32 v207, 16, v50
	v_fmac_f32_e32 v209, v194, v194
	v_and_b32_e32 v205, 0xffff0000, v50
	v_fmac_f32_e32 v209, v207, v207
	v_lshlrev_b32_e32 v203, 16, v51
	v_fmac_f32_e32 v209, v205, v205
	v_and_b32_e32 v200, 0xffff0000, v51
	v_fmac_f32_e32 v209, v203, v203
	v_lshlrev_b32_e32 v208, 16, v52
	v_fmac_f32_e32 v209, v200, v200
	v_and_b32_e32 v206, 0xffff0000, v52
	v_fmac_f32_e32 v209, v208, v208
	v_lshlrev_b32_e32 v204, 16, v53
	v_fmac_f32_e32 v209, v206, v206
	v_and_b32_e32 v226, 0xffff0000, v53
	v_fmac_f32_e32 v209, v204, v204
	v_fmac_f32_e32 v209, v226, v226
	v_fmac_f32_e32 v209, v227, v227
	v_fmac_f32_e32 v209, v228, v228
	v_fmac_f32_e32 v209, v229, v229
	v_fmac_f32_e32 v209, v230, v230
	global_load_dwordx4 v[110:113], v40, s[4:5] offset:16
	global_load_dwordx4 v[114:117], v40, s[4:5]
	global_load_dwordx4 v[102:105], v40, s[4:5] offset:80
	global_load_dwordx4 v[106:109], v40, s[4:5] offset:64
	global_load_dwordx4 v[94:97], v40, s[4:5] offset:144
	global_load_dwordx4 v[98:101], v40, s[4:5] offset:128
	global_load_dwordx4 v[86:89], v40, s[4:5] offset:208
	global_load_dwordx4 v[90:93], v40, s[4:5] offset:192
	global_load_dwordx4 v[78:81], v40, s[4:5] offset:272
	global_load_dwordx4 v[82:85], v40, s[4:5] offset:256
	global_load_dwordx4 v[70:73], v40, s[4:5] offset:336
	global_load_dwordx4 v[74:77], v40, s[4:5] offset:320
	global_load_dwordx4 v[62:65], v40, s[4:5] offset:400
	global_load_dwordx4 v[66:69], v40, s[4:5] offset:384
	global_load_dwordx4 v[54:57], v40, s[4:5] offset:464
	global_load_dwordx4 v[58:61], v40, s[4:5] offset:448
	v_fmac_f32_e32 v209, v231, v231
	v_fmac_f32_e32 v209, v232, v232
	v_fmac_f32_e32 v209, v233, v233
	v_fmac_f32_e32 v209, v234, v234
	s_waitcnt vmcnt(29)
	v_lshlrev_b32_e32 v235, 16, v22
	v_and_b32_e32 v236, 0xffff0000, v22
	v_fmac_f32_e32 v209, v235, v235
	v_lshlrev_b32_e32 v237, 16, v23
	v_fmac_f32_e32 v209, v236, v236
	v_and_b32_e32 v238, 0xffff0000, v23
	v_fmac_f32_e32 v209, v237, v237
	v_lshlrev_b32_e32 v239, 16, v24
	v_fmac_f32_e32 v209, v238, v238
	v_and_b32_e32 v240, 0xffff0000, v24
	v_fmac_f32_e32 v209, v239, v239
	v_lshlrev_b32_e32 v241, 16, v25
	v_fmac_f32_e32 v209, v240, v240
	v_and_b32_e32 v242, 0xffff0000, v25
	v_fmac_f32_e32 v209, v241, v241
	v_fmac_f32_e32 v209, v242, v242
	s_waitcnt vmcnt(28)
	v_lshlrev_b32_e32 v243, 16, v18
	v_and_b32_e32 v244, 0xffff0000, v18
	v_fmac_f32_e32 v209, v243, v243
	v_lshlrev_b32_e32 v245, 16, v19
	v_fmac_f32_e32 v209, v244, v244
	v_and_b32_e32 v246, 0xffff0000, v19
	v_fmac_f32_e32 v209, v245, v245
	v_lshlrev_b32_e32 v247, 16, v20
	v_fmac_f32_e32 v209, v246, v246
	v_and_b32_e32 v248, 0xffff0000, v20
	v_fmac_f32_e32 v209, v247, v247
	v_lshlrev_b32_e32 v249, 16, v21
	v_fmac_f32_e32 v209, v248, v248
	v_and_b32_e32 v250, 0xffff0000, v21
	v_fmac_f32_e32 v209, v249, v249
	s_waitcnt vmcnt(27)
	v_lshlrev_b32_e32 v223, 16, v10
	s_waitcnt vmcnt(25)
	v_lshlrev_b32_e32 v222, 16, v2
	v_fmac_f32_e32 v209, v250, v250
	s_waitcnt vmcnt(18)
	v_mov_b32_e32 v150, v158
	v_mov_b32_e32 v158, v156
	v_lshlrev_b32_e32 v156, 16, v3
	v_and_b32_e32 v160, 0xffff0000, v3
	v_and_b32_e32 v225, 0xffff0000, v10
	v_and_b32_e32 v224, 0xffff0000, v2
	v_pk_mul_f32 v[2:3], v[222:223], v[222:223]
	v_mov_b32_e32 v134, v144
	v_mov_b32_e32 v140, v142
	v_lshlrev_b32_e32 v142, 16, v5
	s_waitcnt vmcnt(17)
	v_mov_b32_e32 v151, v28
	v_and_b32_e32 v144, 0xffff0000, v5
	v_mov_b32_e32 v28, v159
	v_lshlrev_b32_e32 v152, 16, v4
	v_mov_b32_e32 v159, v26
	v_and_b32_e32 v154, 0xffff0000, v4
	v_mov_b32_e32 v26, v157
	v_lshlrev_b32_e32 v157, 16, v11
	v_add_f32_e32 v3, v3, v209
	v_pk_mul_f32 v[4:5], v[224:225], v[224:225]
	v_lshlrev_b32_e32 v119, 16, v45
	v_and_b32_e32 v121, 0xffff0000, v45
	v_lshlrev_b32_e32 v125, 16, v44
	v_and_b32_e32 v127, 0xffff0000, v44
	v_pk_mul_f32 v[44:45], v[156:157], v[156:157]
	v_and_b32_e32 v161, 0xffff0000, v11
	v_add_f32_e32 v3, v5, v3
	v_mov_b32_e32 v122, v132
	v_mov_b32_e32 v128, v130
	v_lshlrev_b32_e32 v130, 16, v47
	v_and_b32_e32 v132, 0xffff0000, v47
	v_lshlrev_b32_e32 v136, 16, v46
	v_and_b32_e32 v138, 0xffff0000, v46
	v_lshlrev_b32_e32 v153, 16, v12
	v_pk_mul_f32 v[46:47], v[160:161], v[160:161]
	v_add_f32_e32 v3, v45, v3
	v_mov_b32_e32 v123, v8
	v_mov_b32_e32 v8, v133
	v_mov_b32_e32 v129, v6
	v_mov_b32_e32 v6, v131
	v_lshlrev_b32_e32 v131, 16, v43
	v_and_b32_e32 v133, 0xffff0000, v43
	v_lshlrev_b32_e32 v137, 16, v42
	v_and_b32_e32 v139, 0xffff0000, v42
	v_pk_mul_f32 v[42:43], v[152:153], v[152:153]
	v_and_b32_e32 v155, 0xffff0000, v12
	v_add_f32_e32 v3, v47, v3
	v_mov_b32_e32 v141, v14
	v_mov_b32_e32 v14, v143
	v_lshlrev_b32_e32 v143, 16, v13
	v_pk_mul_f32 v[220:221], v[154:155], v[154:155]
	v_add_f32_e32 v3, v43, v3
	v_mov_b32_e32 v135, v16
	v_mov_b32_e32 v16, v145
	v_pk_mul_f32 v[216:217], v[142:143], v[142:143]
	v_and_b32_e32 v145, 0xffff0000, v13
	v_add_f32_e32 v3, v221, v3
	v_pk_mul_f32 v[218:219], v[144:145], v[144:145]
	v_add_f32_e32 v3, v217, v3
	v_pk_mul_f32 v[212:213], v[136:137], v[136:137]
	v_add_f32_e32 v3, v219, v3
	v_pk_mul_f32 v[214:215], v[138:139], v[138:139]
	v_add_f32_e32 v3, v213, v3
	v_add_f32_e32 v3, v215, v3
	v_fmac_f32_e32 v3, v131, v131
	v_fmac_f32_e32 v3, v133, v133
	v_fmac_f32_e32 v3, v125, v125
	v_fmac_f32_e32 v3, v127, v127
	v_fmac_f32_e32 v3, v119, v119
	v_fmac_f32_e32 v3, v121, v121
	v_add_f32_e32 v2, v2, v3
	v_add_f32_e32 v43, v4, v2
	v_add_f32_e32 v43, v44, v43
	v_add_f32_e32 v43, v46, v43
	v_add_f32_e32 v209, v42, v43
	v_add_f32_e32 v209, v220, v209
	v_add_f32_e32 v209, v216, v209
	v_add_f32_e32 v209, v218, v209
	v_mov_b32_e32 v218, v132
	v_mov_b32_e32 v219, v130
	v_add_f32_e32 v209, v212, v209
	v_lshlrev_b64 v[18:19], 8, v[38:39]
	v_lshlrev_b32_e32 v124, 16, v48
	v_and_b32_e32 v126, 0xffff0000, v48
	v_pk_mul_f32 v[218:219], v[218:219], v[218:219]
	s_waitcnt vmcnt(16)
	v_mov_b32_e32 v213, v32
	v_add_f32_e32 v32, v214, v209
	v_lshl_add_u64 v[18:19], s[10:11], 0, v[18:19]
	v_lshlrev_b32_e32 v20, 6, v173
	v_mov_b32_e32 v21, v149
	v_mov_b32_e32 v216, v126
	v_mov_b32_e32 v217, v124
	v_add_f32_e32 v32, v219, v32
	v_lshl_add_u64 v[210:211], v[18:19], 0, v[20:21]
	v_lshlrev_b32_e32 v118, 16, v49
	v_and_b32_e32 v120, 0xffff0000, v49
	v_pk_mul_f32 v[216:217], v[216:217], v[216:217]
	v_add_f32_e32 v32, v218, v32
	global_load_dwordx4 v[18:21], v[210:211], off offset:48
	global_load_dwordx4 v[22:25], v[210:211], off offset:32
	global_load_dwordx4 v[38:41], v[210:211], off offset:16
	global_load_dwordx4 v[50:53], v[210:211], off
	global_load_dwordx4 v[2:5], v[210:211], off offset:176
	global_load_dwordx4 v[10:13], v[210:211], off offset:160
	global_load_dwordx4 v[42:45], v[210:211], off offset:144
	global_load_dwordx4 v[46:49], v[210:211], off offset:128
	v_mov_b32_e32 v210, v120
	v_mov_b32_e32 v211, v118
	v_add_f32_e32 v32, v217, v32
	v_pk_mul_f32 v[210:211], v[210:211], v[210:211]
	v_add_f32_e32 v32, v216, v32
	v_add_f32_e32 v32, v211, v32
	v_add_f32_e32 v32, v210, v32
	v_mov_b32_e32 v212, v36
	v_mov_b32_e32 v36, v32
	s_nop 1
	v_permlane32_swap_b32_e32 v32, v36
	v_add_f32_e32 v32, v32, v36
	v_fmamk_f32 v32, v32, 0x3baaaaab, v163
	v_mul_f32_e32 v36, 0x4b800000, v32
	v_cmp_gt_f32_e32 vcc, s69, v32
	s_nop 1
	v_cndmask_b32_e32 v32, v32, v36, vcc
	v_rsq_f32_e32 v209, v32
	v_mov_b32_e32 v32, v37
	v_mov_b32_e32 v37, v30
	v_mov_b32_e32 v36, v34
	v_mul_f32_e32 v30, 0x45800000, v209
	v_cndmask_b32_e32 v30, v209, v30, vcc
	v_mul_f32_e32 v34, 0x3dd53b94, v30
	s_waitcnt vmcnt(22)
	v_mul_f32_e32 v30, v114, v34
	v_mul_f32_e32 v114, v30, v177
	v_mul_f32_e32 v30, v110, v34
	v_mul_f32_e32 v110, v30, v180
	v_mul_f32_e32 v30, v115, v34
	v_mul_f32_e32 v115, v30, v174
	v_mul_f32_e32 v30, v111, v34
	v_mul_f32_e32 v111, v30, v176
	v_mul_f32_e32 v30, v116, v34
	v_mul_f32_e32 v116, v30, v170
	v_mul_f32_e32 v30, v112, v34
	v_mul_f32_e32 v112, v30, v171
	v_mul_f32_e32 v30, v117, v34
	v_mul_f32_e32 v117, v30, v167
	v_mul_f32_e32 v30, v113, v34
	v_mul_f32_e32 v113, v30, v169
	s_waitcnt vmcnt(20)
	v_mul_f32_e32 v30, v106, v34
	v_mul_f32_e32 v106, v30, v185
	v_mul_f32_e32 v30, v102, v34
	v_mul_f32_e32 v167, v30, v187
	v_mul_f32_e32 v30, v107, v34
	v_mul_f32_e32 v102, v30, v182
	v_mul_f32_e32 v30, v103, v34
	v_mul_f32_e32 v107, v30, v183
	v_mul_f32_e32 v30, v108, v34
	v_mul_f32_e32 v103, v30, v179
	v_mul_f32_e32 v30, v104, v34
	v_mul_f32_e32 v108, v30, v181
	v_mul_f32_e32 v30, v109, v34
	v_mul_f32_e32 v104, v30, v175
	v_mul_f32_e32 v30, v105, v34
	v_mul_f32_e32 v105, v30, v178
	s_waitcnt vmcnt(18)
	v_mul_f32_e32 v30, v98, v34
	v_mul_f32_e32 v109, v30, v193
	v_mul_f32_e32 v30, v94, v34
	v_mul_f32_e32 v94, v30, v195
	v_mul_f32_e32 v30, v99, v34
	v_mul_f32_e32 v169, v30, v190
	v_mul_f32_e32 v30, v95, v34
	v_mul_f32_e32 v95, v30, v191
	v_mul_f32_e32 v30, v100, v34
	v_mul_f32_e32 v170, v30, v188
	v_mul_f32_e32 v30, v96, v34
	v_mul_f32_e32 v96, v30, v189
	v_mul_f32_e32 v30, v101, v34
	v_mul_f32_e32 v171, v30, v184
	v_mul_f32_e32 v30, v97, v34
	v_mul_f32_e32 v97, v30, v186
	s_waitcnt vmcnt(16)
	v_mul_f32_e32 v30, v90, v34
	v_mul_f32_e32 v90, v30, v201
	v_mul_f32_e32 v30, v86, v34
	v_mul_f32_e32 v86, v30, v202
	v_mul_f32_e32 v30, v91, v34
	v_mul_f32_e32 v91, v30, v198
	v_mul_f32_e32 v30, v87, v34
	v_mul_f32_e32 v87, v30, v199
	v_mul_f32_e32 v30, v92, v34
	v_mul_f32_e32 v92, v30, v196
	v_mul_f32_e32 v30, v88, v34
	v_mul_f32_e32 v88, v30, v197
	v_mul_f32_e32 v30, v93, v34
	v_mul_f32_e32 v93, v30, v192
	v_mul_f32_e32 v30, v89, v34
	v_mul_f32_e32 v89, v30, v194
	s_waitcnt vmcnt(14)
	v_mul_f32_e32 v30, v82, v34
	v_mul_f32_e32 v82, v30, v207
	v_mul_f32_e32 v30, v34, v78
	v_mul_f32_e32 v78, v30, v208
	v_mul_f32_e32 v30, v83, v34
	v_mul_f32_e32 v83, v30, v205
	v_mul_f32_e32 v30, v34, v79
	v_mul_f32_e32 v79, v30, v206
	v_mul_f32_e32 v30, v84, v34
	v_mul_f32_e32 v84, v30, v203
	v_mul_f32_e32 v30, v34, v80
	v_mul_f32_e32 v80, v30, v204
	v_mul_f32_e32 v30, v85, v34
	v_mul_f32_e32 v85, v30, v200
	v_mul_f32_e32 v30, v34, v81
	v_mul_f32_e32 v81, v30, v226
	s_waitcnt vmcnt(12)
	v_mul_f32_e32 v30, v34, v74
	v_mul_f32_e32 v74, v30, v227
	v_mul_f32_e32 v30, v34, v70
	v_mul_f32_e32 v70, v30, v231
	v_mul_f32_e32 v30, v34, v75
	v_mul_f32_e32 v75, v30, v228
	v_mul_f32_e32 v30, v34, v71
	v_mul_f32_e32 v71, v30, v232
	v_mul_f32_e32 v30, v34, v76
	v_mul_f32_e32 v76, v30, v229
	v_mul_f32_e32 v30, v34, v72
	v_mul_f32_e32 v72, v30, v233
	v_mul_f32_e32 v30, v34, v77
	v_mul_f32_e32 v77, v30, v230
	v_mul_f32_e32 v30, v34, v73
	v_mul_f32_e32 v73, v30, v234
	s_waitcnt vmcnt(10)
	v_mul_f32_e32 v30, v34, v66
	v_mul_f32_e32 v174, v30, v235
	v_mul_f32_e32 v30, v34, v62
	v_mul_f32_e32 v175, v30, v239
	v_mul_f32_e32 v30, v34, v67
	v_mul_f32_e32 v176, v30, v236
	v_mul_f32_e32 v30, v34, v63
	v_mul_f32_e32 v177, v30, v240
	v_mul_f32_e32 v30, v34, v68
	v_mul_f32_e32 v68, v30, v237
	v_mul_f32_e32 v30, v34, v64
	v_mul_f32_e32 v178, v30, v241
	v_mul_f32_e32 v30, v34, v69
	v_mul_f32_e32 v69, v30, v238
	v_mul_f32_e32 v30, v34, v65
	v_mul_f32_e32 v179, v30, v242
	s_waitcnt vmcnt(8)
	v_mul_f32_e32 v30, v34, v58
	v_mul_f32_e32 v180, v30, v243
	v_mul_f32_e32 v30, v34, v54
	v_mul_f32_e32 v181, v30, v247
	v_mul_f32_e32 v30, v34, v59
	v_mul_f32_e32 v182, v30, v244
	v_mul_f32_e32 v30, v34, v55
	v_mul_f32_e32 v183, v30, v248
	v_mul_f32_e32 v30, v34, v60
	v_mul_f32_e32 v184, v30, v245
	v_mul_f32_e32 v30, v34, v56
	v_mul_f32_e32 v185, v30, v249
	v_mul_f32_e32 v30, v34, v61
	v_mul_f32_e32 v186, v30, v246
	v_mul_f32_e32 v30, v34, v57
	v_pk_mul_f32 v[36:37], v[34:35], v[36:37] op_sel_hi:[0,1]
	v_mul_f32_e32 v187, v30, v250
	v_pk_mul_f32 v[36:37], v[36:37], v[222:223]
	v_mov_b32_e32 v30, v35
	v_pk_mul_f32 v[54:55], v[34:35], v[158:159] op_sel_hi:[0,1]
	v_pk_mul_f32 v[30:31], v[34:35], v[30:31] op_sel_hi:[0,1]
	v_pk_mul_f32 v[26:27], v[34:35], v[26:27] op_sel_hi:[0,1]
	v_pk_mul_f32 v[56:57], v[34:35], v[212:213] op_sel_hi:[0,1]
	v_pk_mul_f32 v[58:59], v[34:35], v[150:151] op_sel_hi:[0,1]
	v_pk_mul_f32 v[32:33], v[34:35], v[32:33] op_sel_hi:[0,1]
	v_pk_mul_f32 v[28:29], v[34:35], v[28:29] op_sel_hi:[0,1]
	v_pk_mul_f32 v[60:61], v[34:35], v[140:141] op_sel_hi:[0,1]
	v_pk_mul_f32 v[62:63], v[34:35], v[128:129] op_sel_hi:[0,1]
	v_pk_mul_f32 v[14:15], v[34:35], v[14:15] op_sel_hi:[0,1]
	v_pk_mul_f32 v[6:7], v[34:35], v[6:7] op_sel_hi:[0,1]
	v_pk_mul_f32 v[64:65], v[34:35], v[134:135] op_sel_hi:[0,1]
	v_pk_mul_f32 v[66:67], v[34:35], v[122:123] op_sel_hi:[0,1]
	v_pk_mul_f32 v[16:17], v[34:35], v[16:17] op_sel_hi:[0,1]
	v_pk_mul_f32 v[8:9], v[34:35], v[8:9] op_sel_hi:[0,1]
	s_waitcnt vmcnt(4)
	v_pk_mul_f32 v[34:35], v[36:37], v[50:51] op_sel:[1,0] op_sel_hi:[0,1]
	v_pk_mul_f32 v[30:31], v[30:31], v[224:225]
	v_pk_mul_f32 v[64:65], v[64:65], v[130:131]
	v_sub_f32_e32 v130, v34, v35
	v_pk_mul_f32 v[34:35], v[36:37], v[50:51]
	v_pk_mul_f32 v[56:57], v[56:57], v[156:157]
	v_add_f32_e32 v36, v35, v34
	v_pk_mul_f32 v[34:35], v[30:31], v[52:53] op_sel:[1,0] op_sel_hi:[0,1]
	v_pk_mul_f32 v[30:31], v[30:31], v[52:53]
	v_sub_f32_e32 v34, v34, v35
	v_add_f32_e32 v35, v31, v30
	v_pk_mul_f32 v[30:31], v[56:57], v[38:39] op_sel:[1,0] op_sel_hi:[0,1]
	v_pk_mul_f32 v[32:33], v[32:33], v[160:161]
	v_sub_f32_e32 v37, v30, v31
	v_pk_mul_f32 v[30:31], v[56:57], v[38:39]
	v_pk_mul_f32 v[54:55], v[54:55], v[152:153]
	v_add_f32_e32 v38, v31, v30
	v_pk_mul_f32 v[30:31], v[32:33], v[40:41] op_sel:[1,0] op_sel_hi:[0,1]
	v_sub_f32_e32 v39, v30, v31
	v_pk_mul_f32 v[30:31], v[32:33], v[40:41]
	v_pk_mul_f32 v[26:27], v[26:27], v[154:155]
	v_add_f32_e32 v32, v31, v30
	v_pk_mul_f32 v[30:31], v[54:55], v[22:23] op_sel:[1,0] op_sel_hi:[0,1]
	v_pk_mul_f32 v[22:23], v[54:55], v[22:23]
	v_sub_f32_e32 v30, v30, v31
	v_add_f32_e32 v31, v23, v22
	v_pk_mul_f32 v[22:23], v[26:27], v[24:25] op_sel:[1,0] op_sel_hi:[0,1]
	v_pk_mul_f32 v[58:59], v[58:59], v[142:143]
	v_sub_f32_e32 v33, v22, v23
	v_pk_mul_f32 v[22:23], v[26:27], v[24:25]
	v_pk_mul_f32 v[28:29], v[28:29], v[144:145]
	v_add_f32_e32 v24, v23, v22
	v_pk_mul_f32 v[22:23], v[58:59], v[18:19] op_sel:[1,0] op_sel_hi:[0,1]
	v_pk_mul_f32 v[18:19], v[58:59], v[18:19]
	v_sub_f32_e32 v22, v22, v23
	v_add_f32_e32 v23, v19, v18
	v_pk_mul_f32 v[18:19], v[28:29], v[20:21] op_sel:[1,0] op_sel_hi:[0,1]
	v_pk_mul_f32 v[60:61], v[60:61], v[136:137]
	v_sub_f32_e32 v25, v18, v19
	v_pk_mul_f32 v[18:19], v[28:29], v[20:21]
	v_pk_mul_f32 v[14:15], v[14:15], v[138:139]
	v_add_f32_e32 v20, v19, v18
	s_waitcnt vmcnt(0)
	v_pk_mul_f32 v[18:19], v[60:61], v[46:47] op_sel:[1,0] op_sel_hi:[0,1]
	v_sub_f32_e32 v21, v18, v19
	v_pk_mul_f32 v[18:19], v[60:61], v[46:47]
	v_pk_mul_f32 v[16:17], v[16:17], v[132:133]
	v_add_f32_e32 v26, v19, v18
	v_pk_mul_f32 v[18:19], v[14:15], v[48:49] op_sel:[1,0] op_sel_hi:[0,1]
	v_pk_mul_f32 v[14:15], v[14:15], v[48:49]
	v_sub_f32_e32 v18, v18, v19
	v_add_f32_e32 v19, v15, v14
	v_pk_mul_f32 v[14:15], v[64:65], v[42:43] op_sel:[1,0] op_sel_hi:[0,1]
	v_sub_f32_e32 v27, v14, v15
	v_pk_mul_f32 v[14:15], v[64:65], v[42:43]
	v_pk_mul_f32 v[62:63], v[62:63], v[124:125]
	v_add_f32_e32 v28, v15, v14
	v_pk_mul_f32 v[14:15], v[16:17], v[44:45] op_sel:[1,0] op_sel_hi:[0,1]
	v_sub_f32_e32 v29, v14, v15
	v_pk_mul_f32 v[14:15], v[16:17], v[44:45]
	v_pk_mul_f32 v[6:7], v[6:7], v[126:127]
	v_add_f32_e32 v16, v15, v14
	v_pk_mul_f32 v[14:15], v[62:63], v[10:11] op_sel:[1,0] op_sel_hi:[0,1]
	v_pk_mul_f32 v[10:11], v[62:63], v[10:11]
	v_pk_mul_f32 v[66:67], v[66:67], v[118:119]
	v_sub_f32_e32 v14, v14, v15
	v_add_f32_e32 v15, v11, v10
	v_pk_mul_f32 v[10:11], v[6:7], v[12:13] op_sel:[1,0] op_sel_hi:[0,1]
	v_pk_mul_f32 v[6:7], v[6:7], v[12:13]
	v_pk_mul_f32 v[8:9], v[8:9], v[120:121]
	v_sub_f32_e32 v10, v10, v11
	v_add_f32_e32 v11, v7, v6
	v_pk_mul_f32 v[6:7], v[66:67], v[2:3] op_sel:[1,0] op_sel_hi:[0,1]
	v_pk_mul_f32 v[2:3], v[66:67], v[2:3]
	v_sub_f32_e32 v6, v6, v7
	v_add_f32_e32 v7, v3, v2
	v_pk_mul_f32 v[2:3], v[8:9], v[4:5] op_sel:[1,0] op_sel_hi:[0,1]
	v_sub_f32_e32 v12, v2, v3
	v_pk_mul_f32 v[2:3], v[8:9], v[4:5]
	v_cvt_pk_bf16_f32 v98, v114, v115
	v_cvt_pk_bf16_f32 v99, v116, v117
	v_cvt_pk_bf16_f32 v100, v110, v111
	v_cvt_pk_bf16_f32 v101, v112, v113
	v_cvt_pk_bf16_f32 v102, v106, v102
	s_nop 0
	v_add_f32_e32 v2, v3, v2
	v_cvt_pk_bf16_f32 v103, v103, v104
	v_cvt_pk_bf16_f32 v104, v167, v107
	v_cvt_pk_bf16_f32 v105, v108, v105
	v_cvt_pk_bf16_f32 v106, v109, v169
	v_cvt_pk_bf16_f32 v107, v170, v171
	v_cvt_pk_bf16_f32 v108, v94, v95
	v_cvt_pk_bf16_f32 v109, v96, v97
	v_cvt_pk_bf16_f32 v110, v90, v91
	v_cvt_pk_bf16_f32 v111, v92, v93
	v_cvt_pk_bf16_f32 v112, v86, v87
	v_cvt_pk_bf16_f32 v113, v88, v89
	v_cvt_pk_bf16_f32 v114, v82, v83
	v_cvt_pk_bf16_f32 v115, v84, v85
	v_cvt_pk_bf16_f32 v116, v78, v79
	v_cvt_pk_bf16_f32 v117, v80, v81
	v_cvt_pk_bf16_f32 v118, v74, v75
	v_cvt_pk_bf16_f32 v119, v76, v77
	v_cvt_pk_bf16_f32 v120, v70, v71
	v_cvt_pk_bf16_f32 v121, v72, v73
	v_cvt_pk_bf16_f32 v122, v174, v176
	v_cvt_pk_bf16_f32 v123, v68, v69
	v_cvt_pk_bf16_f32 v124, v175, v177
	v_cvt_pk_bf16_f32 v125, v178, v179
	v_cvt_pk_bf16_f32 v126, v180, v182
	v_cvt_pk_bf16_f32 v127, v184, v186
	v_cvt_pk_bf16_f32 v128, v181, v183
	v_cvt_pk_bf16_f32 v129, v185, v187
	v_cvt_pk_bf16_f32 v130, v130, v34
	v_cvt_pk_bf16_f32 v131, v37, v39
	v_cvt_pk_bf16_f32 v132, v30, v33
	v_cvt_pk_bf16_f32 v133, v22, v25
	v_cvt_pk_bf16_f32 v134, v21, v18
	v_cvt_pk_bf16_f32 v135, v27, v29
	v_cvt_pk_bf16_f32 v136, v14, v10
	v_cvt_pk_bf16_f32 v137, v6, v12
	v_cvt_pk_bf16_f32 v138, v36, v35
	v_cvt_pk_bf16_f32 v139, v38, v32
	v_cvt_pk_bf16_f32 v140, v31, v24
	v_cvt_pk_bf16_f32 v141, v23, v20
	v_cvt_pk_bf16_f32 v142, v26, v19
	v_cvt_pk_bf16_f32 v143, v28, v16
	v_cvt_pk_bf16_f32 v144, v15, v11
	v_cvt_pk_bf16_f32 v145, v7, v2
	v_mul_hi_i32 v2, v172, s70
	v_lshrrev_b32_e32 v3, 31, v2
	v_ashrrev_i32_e32 v2, 2, v2
	v_add_u32_e32 v2, v2, v3
	v_mul_lo_u32 v3, v2, 24
	v_sub_u32_e32 v3, v172, v3
	v_lshrrev_b32_e32 v16, 1, v2
	v_bitop3_b32 v3, v16, v3, 7 bitop3:0x6c
	v_mul_lo_u32 v2, v2, s68
	v_lshl_add_u32 v2, v3, 4, v2
	v_add_u32_e32 v3, 0x200, v172
	v_mul_hi_i32 v4, v3, s70
	v_lshrrev_b32_e32 v5, 31, v4
	v_ashrrev_i32_e32 v4, 2, v4
	v_add_u32_e32 v4, v4, v5
	v_mul_lo_u32 v5, v4, 24
	v_sub_u32_e32 v5, v3, v5
	v_lshrrev_b32_e32 v16, 1, v4
	v_bitop3_b32 v5, v16, v5, 7 bitop3:0x6c
	v_mul_lo_u32 v4, v4, s68
	v_lshl_add_u32 v4, v5, 4, v4
	v_add_u32_e32 v5, 0x400, v172
	v_mul_hi_i32 v6, v5, s70
	v_lshrrev_b32_e32 v7, 31, v6
	v_ashrrev_i32_e32 v6, 2, v6
	v_add_u32_e32 v6, v6, v7
	v_mul_lo_u32 v7, v6, 24
	v_sub_u32_e32 v5, v5, v7
	v_lshrrev_b32_e32 v16, 1, v6
	v_bitop3_b32 v5, v16, v5, 7 bitop3:0x6c
	v_mul_lo_u32 v6, v6, s68
	v_ashrrev_i32_e32 v9, 4, v172
	v_lshl_add_u32 v6, v5, 4, v6
	v_bfe_u32 v5, v172, 2, 2
	v_lshrrev_b32_e32 v7, 1, v172
	v_and_b32_e32 v10, 0x1ffff0, v9
	v_lshrrev_b32_e32 v9, 1, v9
	v_ashrrev_i32_e32 v3, 4, v3
	v_and_or_b32 v5, v7, 8, v5
	v_and_b32_e32 v7, 0x60, v172
	v_lshlrev_b32_e32 v8, 3, v172
	v_and_b32_e32 v9, 4, v9
	v_and_b32_e32 v11, 0x1ffff0, v3
	v_lshrrev_b32_e32 v3, 1, v3
	v_and_or_b32 v7, v8, 24, v7
	v_or3_b32 v9, v10, v9, v5
	v_and_b32_e32 v3, 4, v3
	s_barrier
	global_load_lds_dwordx4 v2, s[44:45]
	s_mov_b32 m0, s72
	v_lshlrev_b32_e32 v7, 1, v7
	v_lshlrev_b32_e32 v10, 11, v9
	v_or3_b32 v3, v11, v3, v5
	global_load_lds_dwordx4 v4, s[44:45]
	s_mov_b32 m0, s73
	v_or_b32_e32 v9, v10, v7
	v_lshlrev_b32_e32 v11, 11, v3
	global_load_lds_dwordx4 v6, s[44:45]
	s_mov_b32 m0, s64
	v_or_b32_e32 v3, v11, v7
	global_load_lds_dwordx4 v9, s[46:47]
	s_mov_b32 m0, s74
	v_lshlrev_b32_e32 v13, 1, v172
	global_load_lds_dwordx4 v3, s[46:47]
	v_lshlrev_b32_e32 v9, 4, v172
	v_and_b32_e32 v14, 32, v13
	v_or_b32_e32 v3, 32, v148
	v_mul_u32_u24_e32 v5, 0x180, v168
	v_and_b32_e32 v7, 0x70, v8
	v_and_b32_e32 v12, 0xc0, v9
	v_and_or_b32 v8, v8, s75, v14
	v_and_b32_e32 v167, 63, v172
	v_bitop3_b32 v169, v3, v5, v7 bitop3:0xde
	v_or_b32_e32 v3, 64, v148
	v_add3_u32 v172, v12, 0, v8
	v_and_b32_e32 v12, 0xc0, v13
	v_and_b32_e32 v13, 48, v9
	v_bitop3_b32 v170, v3, v5, v7 bitop3:0xde
	v_or_b32_e32 v3, 0x60, v148
	v_or3_b32 v8, v11, v12, v13
	v_mov_b32_e32 v9, v149
	v_bitop3_b32 v161, v148, v5, v7 bitop3:0xde
	v_bitop3_b32 v171, v3, v5, v7 bitop3:0xde
	v_mov_b32_e32 v3, v149
	v_mov_b32_e32 v5, v149
	v_mov_b32_e32 v7, v149
	v_mul_i32_i24_e32 v15, -4, v173
	v_lshl_add_u64 v[150:151], s[48:49], 0, v[8:9]
	v_or3_b32 v8, v10, v12, v13
	v_mov_b32_e32 v16, v149
	v_mov_b32_e32 v17, v149
	v_lshl_add_u32 v160, v168, 2, s65
	v_lshl_add_u64 v[152:153], s[48:49], 0, v[8:9]
	v_lshl_add_u64 v[154:155], s[50:51], 0, v[6:7]
	v_lshl_add_u64 v[156:157], s[50:51], 0, v[4:5]
	v_lshl_add_u64 v[158:159], s[50:51], 0, v[2:3]
	v_add3_u32 v168, s63, v15, v168
	v_mov_b32_e32 v2, v149
	v_mov_b32_e32 v4, v149
	v_mov_b32_e32 v6, v149
	v_mov_b32_e32 v8, v149
	v_mov_b32_e32 v10, v149
	v_mov_b32_e32 v11, v149
	v_mov_b32_e32 v12, v149
	v_mov_b32_e32 v13, v149
	v_mov_b32_e32 v14, v149
	v_mov_b32_e32 v15, v149
	v_mov_b64_e32 v[32:33], v[16:17]
	v_mov_b64_e32 v[48:49], v[16:17]
	v_mov_b64_e32 v[64:65], v[16:17]
	v_cmp_gt_u32_e64 s[0:1], 32, v167
	v_mov_b32_e32 v173, 0xf149f2ca
	v_mov_b64_e32 v[30:31], v[14:15]
	v_mov_b64_e32 v[28:29], v[12:13]
	v_mov_b64_e32 v[26:27], v[10:11]
	v_mov_b64_e32 v[24:25], v[8:9]
	v_mov_b64_e32 v[22:23], v[6:7]
	v_mov_b64_e32 v[20:21], v[4:5]
	v_mov_b64_e32 v[18:19], v[2:3]
	v_mov_b64_e32 v[46:47], v[14:15]
	v_mov_b64_e32 v[44:45], v[12:13]
	v_mov_b64_e32 v[42:43], v[10:11]
	v_mov_b64_e32 v[40:41], v[8:9]
	v_mov_b64_e32 v[38:39], v[6:7]
	v_mov_b64_e32 v[36:37], v[4:5]
	v_mov_b64_e32 v[34:35], v[2:3]
	v_mov_b64_e32 v[62:63], v[14:15]
	v_mov_b64_e32 v[60:61], v[12:13]
	v_mov_b64_e32 v[58:59], v[10:11]
	v_mov_b64_e32 v[56:57], v[8:9]
	v_mov_b64_e32 v[54:55], v[6:7]
	v_mov_b64_e32 v[52:53], v[4:5]
	v_mov_b64_e32 v[50:51], v[2:3]
	v_mov_b32_e32 v174, 0
	s_mov_b32 s87, 0xe000
	s_mov_b32 s88, 0x18000
	s_mov_b32 s89, 0x8000
	s_mov_b32 s94, 0
	s_mov_b32 s95, 0x4000
	s_mov_b32 s96, 0x1e000
	s_mov_b32 s97, 0x14000
	s_add_i32 s56, s64, s87
	s_mov_b32 m0, s56
	v_lshl_add_u64 v[66:67], s[2:3], 0, v[158:159]
	global_load_lds_dwordx4 v[66:67], off
	v_lshl_add_u64 v[66:67], s[2:3], 0, v[156:157]
	s_add_i32 m0, s56, 0x2000
	s_nop 0
	global_load_lds_dwordx4 v[66:67], off
	s_add_i32 m0, s56, 0x4000
	v_lshl_add_u64 v[66:67], s[2:3], 0, v[154:155]
	s_add_i32 s56, s64, s95
	global_load_lds_dwordx4 v[66:67], off
	v_lshl_add_u64 v[66:67], s[2:3], 0, v[152:153]
	s_mov_b32 m0, s56
	s_nop 0
	global_load_lds_dwordx4 v[66:67], off
	v_lshl_add_u64 v[66:67], s[2:3], 0, v[150:151]
	s_add_i32 m0, s56, 0x2000
	s_nop 0
	global_load_lds_dwordx4 v[66:67], off
	v_lshl_add_u64 v[150:151], v[150:151], 0, s[14:15]
	v_lshl_add_u64 v[152:153], v[152:153], 0, s[14:15]
	v_lshl_add_u64 v[154:155], v[154:155], 0, s[16:17]
	v_lshl_add_u64 v[156:157], v[156:157], 0, s[16:17]
	v_lshl_add_u64 v[158:159], v[158:159], 0, s[16:17]
	s_add_i32 s56, s64, s88
	s_mov_b32 m0, s56
	v_lshl_add_u64 v[66:67], s[2:3], 0, v[158:159]
	global_load_lds_dwordx4 v[66:67], off
	v_lshl_add_u64 v[66:67], s[2:3], 0, v[156:157]
	s_add_i32 m0, s56, 0x2000
	s_nop 0
	global_load_lds_dwordx4 v[66:67], off
	s_add_i32 m0, s56, 0x4000
	v_lshl_add_u64 v[66:67], s[2:3], 0, v[154:155]
	s_add_i32 s56, s64, s96
	global_load_lds_dwordx4 v[66:67], off
	v_lshl_add_u64 v[66:67], s[2:3], 0, v[152:153]
	s_mov_b32 m0, s56
	s_nop 0
	global_load_lds_dwordx4 v[66:67], off
	v_lshl_add_u64 v[66:67], s[2:3], 0, v[150:151]
	s_add_i32 m0, s56, 0x2000
	s_nop 0
	global_load_lds_dwordx4 v[66:67], off
	v_lshl_add_u64 v[150:151], v[150:151], 0, s[14:15]
	v_lshl_add_u64 v[152:153], v[152:153], 0, s[14:15]
	v_lshl_add_u64 v[154:155], v[154:155], 0, s[16:17]
	v_lshl_add_u64 v[156:157], v[156:157], 0, s[16:17]
	v_lshl_add_u64 v[158:159], v[158:159], 0, s[16:17]
	s_waitcnt vmcnt(10)
	s_waitcnt lgkmcnt(0)
	s_barrier
	s_movk_i32 s56, 0x0
	s_add_i32 s56, s56, 0
	s_add_i32 s56, s56, 0x8000
	v_add_u32_e32 v175, s56, v161
	ds_read_b128 v[66:69], v175 offset:0
	ds_read_b128 v[70:73], v175 offset:0x3000
	v_add_u32_e32 v200, s56, v169
	ds_read_b128 v[176:179], v200 offset:0
	ds_read_b128 v[180:183], v200 offset:0x3000
	v_add_u32_e32 v201, s56, v170
	ds_read_b128 v[184:187], v201 offset:0
	ds_read_b128 v[188:191], v201 offset:0x3000
	s_waitcnt lgkmcnt(4)
	v_add_u32_e32 v202, s56, v171
	v_mfma_f32_32x32x16_bf16 v[82:97], v[66:69], v[98:101], 0
	ds_read_b128 v[192:195], v202 offset:0
	ds_read_b128 v[196:199], v202 offset:0x3000
	s_waitcnt lgkmcnt(4)
	v_mfma_f32_32x32x16_bf16 v[66:81], v[70:73], v[98:101], 0
	v_mfma_f32_32x32x16_bf16 v[82:97], v[176:179], v[102:105], v[82:97]
	ds_read_b128 v[176:179], v175 offset:0x80
	v_mfma_f32_32x32x16_bf16 v[66:81], v[180:183], v[102:105], v[66:81]
	ds_read_b128 v[180:183], v175 offset:0x3080
	s_waitcnt lgkmcnt(4)
	v_mfma_f32_32x32x16_bf16 v[82:97], v[184:187], v[106:109], v[82:97]
	ds_read_b128 v[184:187], v200 offset:0x80
	v_mfma_f32_32x32x16_bf16 v[66:81], v[188:191], v[106:109], v[66:81]
	ds_read_b128 v[188:191], v200 offset:0x3080
	s_waitcnt lgkmcnt(4)
	v_mfma_f32_32x32x16_bf16 v[82:97], v[192:195], v[110:113], v[82:97]
	ds_read_b128 v[192:195], v201 offset:0x80
	v_mfma_f32_32x32x16_bf16 v[66:81], v[196:199], v[110:113], v[66:81]
	ds_read_b128 v[196:199], v201 offset:0x3080
	s_waitcnt lgkmcnt(4)
	v_mfma_f32_32x32x16_bf16 v[82:97], v[176:179], v[114:117], v[82:97]
	ds_read_b128 v[176:179], v202 offset:0x80
	v_mfma_f32_32x32x16_bf16 v[66:81], v[180:183], v[114:117], v[66:81]
	ds_read_b128 v[180:183], v202 offset:0x3080
	s_waitcnt lgkmcnt(4)
	v_mfma_f32_32x32x16_bf16 v[82:97], v[184:187], v[118:121], v[82:97]
	ds_read_b128 v[184:187], v175 offset:0x100
	v_mfma_f32_32x32x16_bf16 v[66:81], v[188:191], v[118:121], v[66:81]
	ds_read_b128 v[188:191], v175 offset:0x3100
	s_waitcnt lgkmcnt(4)
	v_mfma_f32_32x32x16_bf16 v[82:97], v[192:195], v[122:125], v[82:97]
	ds_read_b128 v[192:195], v200 offset:0x100
	v_mfma_f32_32x32x16_bf16 v[66:81], v[196:199], v[122:125], v[66:81]
	ds_read_b128 v[196:199], v200 offset:0x3100
	s_waitcnt lgkmcnt(4)
	v_mfma_f32_32x32x16_bf16 v[82:97], v[176:179], v[126:129], v[82:97]
	ds_read_b128 v[176:179], v201 offset:0x100
	v_mfma_f32_32x32x16_bf16 v[66:81], v[180:183], v[126:129], v[66:81]
	ds_read_b128 v[180:183], v201 offset:0x3100
	s_waitcnt lgkmcnt(4)
	v_mfma_f32_32x32x16_bf16 v[82:97], v[184:187], v[130:133], v[82:97]
	ds_read_b128 v[184:187], v202 offset:0x100
	v_mfma_f32_32x32x16_bf16 v[66:81], v[188:191], v[130:133], v[66:81]
	ds_read_b128 v[188:191], v202 offset:0x3100
	s_waitcnt lgkmcnt(4)
	v_mfma_f32_32x32x16_bf16 v[82:97], v[192:195], v[134:137], v[82:97]
	s_waitcnt lgkmcnt(2)
	v_mfma_f32_32x32x16_bf16 v[66:81], v[196:199], v[134:137], v[66:81]
	v_mfma_f32_32x32x16_bf16 v[82:97], v[176:179], v[138:141], v[82:97]
	s_waitcnt lgkmcnt(0)
	v_mfma_f32_32x32x16_bf16 v[66:81], v[180:183], v[138:141], v[66:81]
	v_mfma_f32_32x32x16_bf16 v[82:97], v[184:187], v[142:145], v[82:97]
	v_mfma_f32_32x32x16_bf16 v[66:81], v[188:191], v[142:145], v[66:81]
.LBB0_805:
	s_add_i32 s56, s12, 1
	s_cmp_lt_u32 s56, s85
	s_cbranch_scc0 .Latt1_w0
	s_waitcnt vmcnt(5)
	s_branch .Latt1_w1

.Latt1_w1:
	s_add_i32 s56, s12, 2
	s_cmp_ge_u32 s56, s85
	s_waitcnt lgkmcnt(0)
	s_barrier
	s_cbranch_scc1 .Latt1_nodma
	s_add_i32 s56, s64, s89
	s_mov_b32 m0, s56
	v_lshl_add_u64 v[204:205], s[2:3], 0, v[158:159]
	global_load_lds_dwordx4 v[204:205], off
	v_lshl_add_u64 v[204:205], s[2:3], 0, v[156:157]
	s_add_i32 m0, s56, 0x2000
	s_nop 0
	global_load_lds_dwordx4 v[204:205], off
	s_add_i32 m0, s56, 0x4000
	v_lshl_add_u64 v[204:205], s[2:3], 0, v[154:155]
	s_add_i32 s56, s64, s97
	global_load_lds_dwordx4 v[204:205], off
	v_lshl_add_u64 v[204:205], s[2:3], 0, v[152:153]
	s_mov_b32 m0, s56
	s_nop 0
	global_load_lds_dwordx4 v[204:205], off
	v_lshl_add_u64 v[204:205], s[2:3], 0, v[150:151]
	s_add_i32 m0, s56, 0x2000
	s_nop 0
	global_load_lds_dwordx4 v[204:205], off
.Latt1_nodma:
	s_add_i32 s56, s86, 0x13f
	s_cmp_le_i32 s56, s84
	s_cbranch_scc1 .Latt1_nomask
	v_add_u32_e32 v175, s83, v168
	v_cmp_lt_i32_e32 vcc, -1, v175
	v_add_u32_e32 v176, -1, v175
	s_nop 4
	v_cndmask_b32_e32 v82, v165, v82, vcc
	v_cmp_lt_i32_e32 vcc, 31, v175
	s_nop 1
	v_cndmask_b32_e32 v66, v165, v66, vcc
	v_cmp_lt_i32_e32 vcc, -1, v176
	s_nop 1
	v_cndmask_b32_e32 v83, v165, v83, vcc
	v_cmp_lt_i32_e32 vcc, 31, v176
	v_add_u32_e32 v176, -2, v175
	s_nop 0
	v_cndmask_b32_e32 v67, v165, v67, vcc
	v_cmp_lt_i32_e32 vcc, -1, v176
	s_nop 1
	v_cndmask_b32_e32 v84, v165, v84, vcc
	v_cmp_lt_i32_e32 vcc, 31, v176
	v_add_u32_e32 v176, -3, v175
	s_nop 0
	v_cndmask_b32_e32 v68, v165, v68, vcc
	v_cmp_lt_i32_e32 vcc, -1, v176
	s_nop 1
	v_cndmask_b32_e32 v85, v165, v85, vcc
	v_cmp_lt_i32_e32 vcc, 31, v176
	v_add_u32_e32 v176, -8, v175
	s_nop 0
	v_cndmask_b32_e32 v69, v165, v69, vcc
	v_cmp_lt_i32_e32 vcc, -1, v176
	s_nop 1
	v_cndmask_b32_e32 v86, v165, v86, vcc
	v_cmp_lt_i32_e32 vcc, 31, v176
	v_add_u32_e32 v176, -9, v175
	s_nop 0
	v_cndmask_b32_e32 v70, v165, v70, vcc
	v_cmp_lt_i32_e32 vcc, -1, v176
	s_nop 1
	v_cndmask_b32_e32 v87, v165, v87, vcc
	v_cmp_lt_i32_e32 vcc, 31, v176
	v_add_u32_e32 v176, -10, v175
	s_nop 0
	v_cndmask_b32_e32 v71, v165, v71, vcc
	v_cmp_lt_i32_e32 vcc, -1, v176
	s_nop 1
	v_cndmask_b32_e32 v88, v165, v88, vcc
	v_cmp_lt_i32_e32 vcc, 31, v176
	v_add_u32_e32 v176, -11, v175
	s_nop 0
	v_cndmask_b32_e32 v72, v165, v72, vcc
	v_cmp_lt_i32_e32 vcc, -1, v176
	s_nop 1
	v_cndmask_b32_e32 v89, v165, v89, vcc
	v_cmp_lt_i32_e32 vcc, 31, v176
	v_add_u32_e32 v176, -16, v175
	s_nop 0
	v_cndmask_b32_e32 v73, v165, v73, vcc
	v_cmp_lt_i32_e32 vcc, -1, v176
	s_nop 1
	v_cndmask_b32_e32 v90, v165, v90, vcc
	v_cmp_lt_i32_e32 vcc, 31, v176
	v_subrev_u32_e32 v176, 17, v175
	s_nop 0
	v_cndmask_b32_e32 v74, v165, v74, vcc
	v_cmp_lt_i32_e32 vcc, -1, v176
	s_nop 1
	v_cndmask_b32_e32 v91, v165, v91, vcc
	v_cmp_lt_i32_e32 vcc, 31, v176
	v_subrev_u32_e32 v176, 18, v175
	s_nop 0
	v_cndmask_b32_e32 v75, v165, v75, vcc
	v_cmp_lt_i32_e32 vcc, -1, v176
	s_nop 1
	v_cndmask_b32_e32 v92, v165, v92, vcc
	v_cmp_lt_i32_e32 vcc, 31, v176
	v_subrev_u32_e32 v176, 19, v175
	s_nop 0
	v_cndmask_b32_e32 v76, v165, v76, vcc
	v_cmp_lt_i32_e32 vcc, -1, v176
	s_nop 1
	v_cndmask_b32_e32 v93, v165, v93, vcc
	v_cmp_lt_i32_e32 vcc, 31, v176
	v_subrev_u32_e32 v176, 24, v175
	s_nop 0
	v_cndmask_b32_e32 v77, v165, v77, vcc
	v_cmp_lt_i32_e32 vcc, -1, v176
	s_nop 1
	v_cndmask_b32_e32 v94, v165, v94, vcc
	v_cmp_lt_i32_e32 vcc, 31, v176
	v_subrev_u32_e32 v176, 25, v175
	s_nop 0
	v_cndmask_b32_e32 v78, v165, v78, vcc
	v_cmp_lt_i32_e32 vcc, -1, v176
	s_nop 1
	v_cndmask_b32_e32 v95, v165, v95, vcc
	v_cmp_lt_i32_e32 vcc, 31, v176
	v_subrev_u32_e32 v176, 26, v175
	v_subrev_u32_e32 v175, 27, v175
	v_cndmask_b32_e32 v79, v165, v79, vcc
	v_cmp_lt_i32_e32 vcc, -1, v176
	s_nop 1
	v_cndmask_b32_e32 v96, v165, v96, vcc
	v_cmp_lt_i32_e32 vcc, 31, v176
	s_nop 1
	v_cndmask_b32_e32 v80, v165, v80, vcc
	v_cmp_lt_i32_e32 vcc, -1, v175
	s_nop 1
	v_cndmask_b32_e32 v97, v165, v97, vcc
	v_cmp_lt_i32_e32 vcc, 31, v175
	s_nop 1
	v_cndmask_b32_e32 v81, v165, v81, vcc
.Latt1_nomask:
	s_cmp_ge_u32 s12, s85
	s_cbranch_scc1 .Latt1_final
	s_mov_b32 s56, s87
	v_add_u32_e32 v203, s56, v161
	ds_read_b128 v[238:241], v203 offset:0
	ds_read_b128 v[242:245], v203 offset:0x3000
	v_add_u32_e32 v200, s56, v169
	ds_read_b128 v[246:249], v200 offset:0
	ds_read_b128 v[180:183], v200 offset:0x3000
	v_add_u32_e32 v201, s56, v170
	ds_read_b128 v[184:187], v201 offset:0
	ds_read_b128 v[188:191], v201 offset:0x3000
	s_waitcnt lgkmcnt(4)
	v_add_u32_e32 v202, s56, v171
	v_mfma_f32_32x32x16_bf16 v[206:221], v[238:241], v[98:101], 0
	s_nop 7
	v_max_f32_e32 v175, v83, v83
	v_max_f32_e32 v176, v82, v82
	v_max_f32_e32 v175, v176, v175
	v_max3_f32 v175, v175, v84, v85
	v_max3_f32 v175, v175, v86, v87
	ds_read_b128 v[192:195], v202 offset:0
	ds_read_b128 v[196:199], v202 offset:0x3000
	s_waitcnt lgkmcnt(4)
	v_mfma_f32_32x32x16_bf16 v[222:237], v[242:245], v[98:101], 0
	v_max3_f32 v175, v175, v88, v89
	v_max3_f32 v175, v175, v90, v91
	v_max3_f32 v175, v175, v92, v93
	v_max3_f32 v175, v175, v94, v95
	v_max3_f32 v175, v175, v96, v97
	v_max3_f32 v175, v175, v66, v67
	v_mfma_f32_32x32x16_bf16 v[206:221], v[246:249], v[102:105], v[206:221]
	v_max3_f32 v175, v175, v68, v69
	v_max3_f32 v175, v175, v70, v71
	v_max3_f32 v175, v175, v72, v73
	v_max3_f32 v175, v175, v74, v75
	v_max3_f32 v175, v175, v76, v77
	v_max3_f32 v175, v175, v78, v79
	ds_read_b128 v[246:249], v203 offset:0x80
	v_mfma_f32_32x32x16_bf16 v[222:237], v[180:183], v[102:105], v[222:237]
	v_max3_f32 v175, v175, v80, v81
	v_mov_b32_e32 v176, v175
	s_nop 1
	v_permlane32_swap_b32_e32 v175, v176
	v_max_f32_e32 v176, v176, v176
	v_max_f32_e32 v175, v175, v175
	ds_read_b128 v[180:183], v203 offset:0x3080
	s_waitcnt lgkmcnt(4)
	v_mfma_f32_32x32x16_bf16 v[206:221], v[184:187], v[106:109], v[206:221]
	v_max_f32_e32 v175, v175, v176
	v_sub_f32_e32 v176, v175, v173
	v_cmp_ge_f32_e32 vcc, s76, v176
	s_cmp_eq_u64 vcc, exec
	v_max_f32_e32 v176, v173, v173
	v_max_f32_e32 v175, v176, v175
	ds_read_b128 v[184:187], v200 offset:0x80
	v_mfma_f32_32x32x16_bf16 v[222:237], v[188:191], v[106:109], v[222:237]
	s_cselect_b64 vcc, -1, 0
	v_sub_f32_e32 v176, v173, v175
	v_cndmask_b32_e32 v173, v175, v173, vcc
	v_sub_f32_e32 v82, v82, v173
	v_sub_f32_e32 v66, v66, v173
	v_exp_f32_e32 v82, v82
	ds_read_b128 v[188:191], v200 offset:0x3080
	s_waitcnt lgkmcnt(4)
	v_mfma_f32_32x32x16_bf16 v[206:221], v[192:195], v[110:113], v[206:221]
	v_exp_f32_e32 v66, v66
	v_sub_f32_e32 v83, v83, v173
	v_sub_f32_e32 v67, v67, v173
	v_exp_f32_e32 v175, v83
	v_exp_f32_e32 v67, v67
	v_sub_f32_e32 v84, v84, v173
	ds_read_b128 v[192:195], v201 offset:0x80
	v_mfma_f32_32x32x16_bf16 v[222:237], v[196:199], v[110:113], v[222:237]
	v_sub_f32_e32 v68, v68, v173
	v_exp_f32_e32 v84, v84
	v_exp_f32_e32 v68, v68
	v_sub_f32_e32 v85, v85, v173
	v_sub_f32_e32 v69, v69, v173
	v_exp_f32_e32 v85, v85
	ds_read_b128 v[196:199], v201 offset:0x3080
	s_waitcnt lgkmcnt(4)
	v_mfma_f32_32x32x16_bf16 v[206:221], v[246:249], v[114:117], v[206:221]
	v_exp_f32_e32 v69, v69
	v_sub_f32_e32 v86, v86, v173
	v_sub_f32_e32 v70, v70, v173
	v_add_f32_e32 v83, v66, v82
	v_exp_f32_e32 v86, v86
	v_exp_f32_e32 v70, v70
	ds_read_b128 v[246:249], v202 offset:0x80
	v_mfma_f32_32x32x16_bf16 v[222:237], v[180:183], v[114:117], v[222:237]
	v_exp_f32_e32 v177, v176
	v_add_f32_e32 v83, 0, v83
	v_add_f32_e32 v176, v67, v175
	v_add_f32_e32 v83, v176, v83
	v_add_f32_e32 v176, v68, v84
	v_add_f32_e32 v83, v176, v83
	ds_read_b128 v[180:183], v202 offset:0x3080
	s_waitcnt lgkmcnt(4)
	v_mfma_f32_32x32x16_bf16 v[206:221], v[184:187], v[118:121], v[206:221]
	v_add_f32_e32 v176, v69, v85
	v_sub_f32_e32 v87, v87, v173
	v_sub_f32_e32 v71, v71, v173
	v_add_f32_e32 v83, v176, v83
	v_add_f32_e32 v176, v70, v86
	v_exp_f32_e32 v87, v87
	ds_read_b128 v[184:187], v203 offset:0x100
	v_mfma_f32_32x32x16_bf16 v[222:237], v[188:191], v[118:121], v[222:237]
	v_exp_f32_e32 v71, v71
	v_add_f32_e32 v178, v176, v83
	v_sub_f32_e32 v83, v88, v173
	v_sub_f32_e32 v72, v72, v173
	v_exp_f32_e32 v88, v83
	v_exp_f32_e32 v72, v72
	ds_read_b128 v[188:191], v203 offset:0x3100
	s_waitcnt lgkmcnt(4)
	v_mfma_f32_32x32x16_bf16 v[206:221], v[192:195], v[122:125], v[206:221]
	v_add_f32_e32 v179, v71, v87
	v_sub_f32_e32 v83, v89, v173
	v_sub_f32_e32 v73, v73, v173
	v_exp_f32_e32 v176, v83
	v_exp_f32_e32 v83, v73
	v_add_f32_e32 v73, v179, v178
	ds_read_b128 v[192:195], v200 offset:0x100
	v_mfma_f32_32x32x16_bf16 v[222:237], v[196:199], v[122:125], v[222:237]
	v_add_f32_e32 v89, v72, v88
	v_add_f32_e32 v178, v89, v73
	v_sub_f32_e32 v73, v90, v173
	v_exp_f32_e32 v89, v73
	v_sub_f32_e32 v73, v74, v173
	v_exp_f32_e32 v73, v73
	ds_read_b128 v[196:199], v200 offset:0x3100
	s_waitcnt lgkmcnt(4)
	v_mfma_f32_32x32x16_bf16 v[206:221], v[246:249], v[126:129], v[206:221]
	v_add_f32_e32 v179, v83, v176
	v_sub_f32_e32 v74, v91, v173
	v_exp_f32_e32 v90, v74
	v_sub_f32_e32 v74, v75, v173
	v_add_f32_e32 v75, v179, v178
	v_add_f32_e32 v91, v73, v89
	ds_read_b128 v[246:249], v201 offset:0x100
	v_mfma_f32_32x32x16_bf16 v[222:237], v[180:183], v[126:129], v[222:237]
	v_add_f32_e32 v178, v91, v75
	v_sub_f32_e32 v75, v92, v173
	v_exp_f32_e32 v74, v74
	v_exp_f32_e32 v91, v75
	v_sub_f32_e32 v75, v76, v173
	v_exp_f32_e32 v75, v75
	ds_read_b128 v[180:183], v201 offset:0x3100
	s_waitcnt lgkmcnt(4)
	v_mfma_f32_32x32x16_bf16 v[206:221], v[184:187], v[130:133], v[206:221]
	v_add_f32_e32 v179, v74, v90
	v_sub_f32_e32 v76, v93, v173
	v_exp_f32_e32 v92, v76
	v_sub_f32_e32 v76, v77, v173
	v_add_f32_e32 v77, v179, v178
	v_add_f32_e32 v93, v75, v91
	ds_read_b128 v[184:187], v202 offset:0x100
	v_mfma_f32_32x32x16_bf16 v[222:237], v[188:191], v[130:133], v[222:237]
	v_add_f32_e32 v178, v93, v77
	v_sub_f32_e32 v77, v94, v173
	v_exp_f32_e32 v76, v76
	v_exp_f32_e32 v93, v77
	v_sub_f32_e32 v77, v78, v173
	v_exp_f32_e32 v77, v77
	ds_read_b128 v[188:191], v202 offset:0x3100
	s_waitcnt lgkmcnt(4)
	v_mfma_f32_32x32x16_bf16 v[206:221], v[192:195], v[134:137], v[206:221]
	v_add_f32_e32 v179, v76, v92
	v_sub_f32_e32 v78, v95, v173
	v_exp_f32_e32 v94, v78
	v_sub_f32_e32 v78, v79, v173
	v_add_f32_e32 v79, v179, v178
	v_add_f32_e32 v95, v77, v93
	s_waitcnt lgkmcnt(2)
	v_mfma_f32_32x32x16_bf16 v[222:237], v[196:199], v[134:137], v[222:237]
	v_exp_f32_e32 v78, v78
	v_add_f32_e32 v79, v95, v79
	v_sub_f32_e32 v95, v96, v173
	v_sub_f32_e32 v80, v80, v173
	v_exp_f32_e32 v95, v95
	v_exp_f32_e32 v80, v80
	v_mfma_f32_32x32x16_bf16 v[206:221], v[246:249], v[138:141], v[206:221]
	v_sub_f32_e32 v96, v97, v173
	v_sub_f32_e32 v81, v81, v173
	v_exp_f32_e32 v96, v96
	v_exp_f32_e32 v81, v81
	v_add_f32_e32 v178, v78, v94
	v_add_f32_e32 v79, v178, v79
	s_waitcnt lgkmcnt(0)
	v_mfma_f32_32x32x16_bf16 v[222:237], v[180:183], v[138:141], v[222:237]
	v_add_f32_e32 v97, v80, v95
	v_add_f32_e32 v79, v97, v79
	v_add_f32_e32 v97, v81, v96
	v_add_f32_e32 v79, v97, v79
	v_cndmask_b32_e64 v97, v177, 1.0, vcc
	v_mov_b32_e32 v177, v79
	v_mfma_f32_32x32x16_bf16 v[206:221], v[184:187], v[142:145], v[206:221]
	s_nop 1
	v_permlane32_swap_b32_e32 v79, v177
	v_cmp_gt_f32_e32 vcc, 1.0, v97
	v_mfma_f32_32x32x16_bf16 v[222:237], v[188:191], v[142:145], v[222:237]
	s_cbranch_vccz .Latt1_noresc
	s_and_saveexec_b64 s[56:57], s[0:1]
	ds_write_b32 v160, v97
	s_or_b64 exec, exec, s[56:57]
	s_waitcnt lgkmcnt(0)
	v_add_u32_e32 v190, s65, v148
	ds_read_b128 v[178:181], v190 offset:96
	ds_read_b128 v[182:185], v190 offset:64
	ds_read_b128 v[186:189], v190 offset:32
	ds_read_b128 v[190:193], v190
	s_waitcnt lgkmcnt(0)
	v_pk_mul_f32 v[62:63], v[62:63], v[178:179]
	v_pk_mul_f32 v[58:59], v[58:59], v[182:183]
	v_pk_mul_f32 v[54:55], v[54:55], v[186:187]
	v_pk_mul_f32 v[64:65], v[64:65], v[180:181]
	v_pk_mul_f32 v[60:61], v[60:61], v[184:185]
	v_pk_mul_f32 v[56:57], v[56:57], v[188:189]
	v_pk_mul_f32 v[52:53], v[52:53], v[192:193]
	v_pk_mul_f32 v[50:51], v[50:51], v[190:191]
	v_pk_mul_f32 v[46:47], v[46:47], v[178:179]
	v_pk_mul_f32 v[42:43], v[42:43], v[182:183]
	v_pk_mul_f32 v[38:39], v[38:39], v[186:187]
	v_pk_mul_f32 v[48:49], v[48:49], v[180:181]
	v_pk_mul_f32 v[44:45], v[44:45], v[184:185]
	v_pk_mul_f32 v[40:41], v[40:41], v[188:189]
	v_pk_mul_f32 v[36:37], v[36:37], v[192:193]
	v_pk_mul_f32 v[34:35], v[34:35], v[190:191]
	v_pk_mul_f32 v[30:31], v[30:31], v[178:179]
	v_pk_mul_f32 v[26:27], v[26:27], v[182:183]
	v_pk_mul_f32 v[22:23], v[22:23], v[186:187]
	v_pk_mul_f32 v[32:33], v[32:33], v[180:181]
	v_pk_mul_f32 v[28:29], v[28:29], v[184:185]
	v_pk_mul_f32 v[24:25], v[24:25], v[188:189]
	v_pk_mul_f32 v[20:21], v[20:21], v[192:193]
	v_pk_mul_f32 v[18:19], v[18:19], v[190:191]
	v_pk_mul_f32 v[14:15], v[14:15], v[178:179]
	v_pk_mul_f32 v[10:11], v[10:11], v[182:183]
	v_pk_mul_f32 v[6:7], v[6:7], v[186:187]
	v_pk_mul_f32 v[16:17], v[16:17], v[180:181]
	v_pk_mul_f32 v[12:13], v[12:13], v[184:185]
	v_pk_mul_f32 v[8:9], v[8:9], v[188:189]
	v_pk_mul_f32 v[4:5], v[4:5], v[192:193]
	v_pk_mul_f32 v[2:3], v[2:3], v[190:191]
.Latt1_noresc:
	v_cvt_pk_bf16_f32 v178, v82, v175
	v_cvt_pk_bf16_f32 v179, v84, v85
	v_cvt_pk_bf16_f32 v180, v86, v87
	v_cvt_pk_bf16_f32 v181, v88, v176
	v_cvt_pk_bf16_f32 v84, v89, v90
	v_cvt_pk_bf16_f32 v85, v91, v92
	v_cvt_pk_bf16_f32 v86, v93, v94
	v_cvt_pk_bf16_f32 v87, v95, v96
	v_cvt_pk_bf16_f32 v66, v66, v67
	v_cvt_pk_bf16_f32 v67, v68, v69
	v_cvt_pk_bf16_f32 v68, v70, v71
	v_cvt_pk_bf16_f32 v69, v72, v83
	v_cvt_pk_bf16_f32 v70, v73, v74
	v_cvt_pk_bf16_f32 v71, v75, v76
	v_cvt_pk_bf16_f32 v72, v77, v78
	v_cvt_pk_bf16_f32 v73, v80, v81
	v_add_u32_e32 v78, s94, v172
	ds_read_b64_tr_b16 v[74:75], v78 offset:0
	ds_read_b64_tr_b16 v[76:77], v78 offset:0x800
	ds_read_b64_tr_b16 v[80:81], v78 offset:0x1000
	ds_read_b64_tr_b16 v[82:83], v78 offset:0x1800
	ds_read_b64_tr_b16 v[88:89], v78 offset:0x2000
	ds_read_b64_tr_b16 v[90:91], v78 offset:0x2800
	ds_read_b64_tr_b16 v[92:93], v78 offset:0x3000
	v_add_f32_e32 v79, v79, v177
	ds_read_b64_tr_b16 v[94:95], v78 offset:0x3800
	v_fmac_f32_e32 v79, v174, v97
	ds_read_b64_tr_b16 v[174:175], v78 offset:0x200
	ds_read_b64_tr_b16 v[176:177], v78 offset:0xa00
	ds_read_b64_tr_b16 v[182:183], v78 offset:0x1200
	ds_read_b64_tr_b16 v[184:185], v78 offset:0x1a00
	ds_read_b64_tr_b16 v[186:187], v78 offset:0x2200
	ds_read_b64_tr_b16 v[188:189], v78 offset:0x2a00
	ds_read_b64_tr_b16 v[190:191], v78 offset:0x3200
	ds_read_b64_tr_b16 v[192:193], v78 offset:0x3a00
	s_waitcnt lgkmcnt(8)
	v_permlane32_swap_b32_e32 v178, v180
	v_permlane32_swap_b32_e32 v179, v181
	v_permlane32_swap_b32_e32 v84, v86
	v_permlane32_swap_b32_e32 v85, v87
	v_permlane32_swap_b32_e32 v66, v68
	v_permlane32_swap_b32_e32 v67, v69
	v_permlane32_swap_b32_e32 v70, v72
	v_permlane32_swap_b32_e32 v71, v73
	v_mfma_f32_32x32x16_bf16 v[50:65], v[178:181], v[74:77], v[50:65]
	ds_read_b64_tr_b16 v[74:75], v78 offset:0x400
	ds_read_b64_tr_b16 v[76:77], v78 offset:0xc00
	v_mfma_f32_32x32x16_bf16 v[50:65], v[84:87], v[80:83], v[50:65]
	ds_read_b64_tr_b16 v[80:81], v78 offset:0x1400
	ds_read_b64_tr_b16 v[82:83], v78 offset:0x1c00
	v_mfma_f32_32x32x16_bf16 v[50:65], v[66:69], v[88:91], v[50:65]
	ds_read_b64_tr_b16 v[88:89], v78 offset:0x2400
	ds_read_b64_tr_b16 v[90:91], v78 offset:0x2c00
	v_mfma_f32_32x32x16_bf16 v[50:65], v[70:73], v[92:95], v[50:65]
	ds_read_b64_tr_b16 v[92:93], v78 offset:0x3400
	ds_read_b64_tr_b16 v[94:95], v78 offset:0x3c00
	s_waitcnt lgkmcnt(8)
	v_mfma_f32_32x32x16_bf16 v[34:49], v[178:181], v[174:177], v[34:49]
	ds_read_b64_tr_b16 v[174:175], v78 offset:0x600
	ds_read_b64_tr_b16 v[176:177], v78 offset:0xe00
	v_mfma_f32_32x32x16_bf16 v[34:49], v[84:87], v[182:185], v[34:49]
	ds_read_b64_tr_b16 v[182:183], v78 offset:0x1600
	ds_read_b64_tr_b16 v[184:185], v78 offset:0x1e00
	v_mfma_f32_32x32x16_bf16 v[34:49], v[66:69], v[186:189], v[34:49]
	ds_read_b64_tr_b16 v[186:187], v78 offset:0x2600
	ds_read_b64_tr_b16 v[188:189], v78 offset:0x2e00
	v_mfma_f32_32x32x16_bf16 v[34:49], v[70:73], v[190:193], v[34:49]
	ds_read_b64_tr_b16 v[190:191], v78 offset:0x3600
	ds_read_b64_tr_b16 v[192:193], v78 offset:0x3e00
	s_waitcnt lgkmcnt(8)
	v_mfma_f32_32x32x16_bf16 v[18:33], v[178:181], v[74:77], v[18:33]
	s_waitcnt lgkmcnt(0)
	v_mfma_f32_32x32x16_bf16 v[18:33], v[84:87], v[80:83], v[18:33]
	v_mfma_f32_32x32x16_bf16 v[18:33], v[66:69], v[88:91], v[18:33]
	v_mfma_f32_32x32x16_bf16 v[18:33], v[70:73], v[92:95], v[18:33]
	v_mfma_f32_32x32x16_bf16 v[2:17], v[178:181], v[174:177], v[2:17]
	s_add_i32 s86, s86, 64
	s_add_i32 s12, s12, 1
	v_lshl_add_u64 v[150:151], v[150:151], 0, s[14:15]
	v_lshl_add_u64 v[152:153], v[152:153], 0, s[14:15]
	v_lshl_add_u64 v[154:155], v[154:155], 0, s[16:17]
	v_lshl_add_u64 v[156:157], v[156:157], 0, s[16:17]
	v_lshl_add_u64 v[158:159], v[158:159], 0, s[16:17]
	v_mfma_f32_32x32x16_bf16 v[2:17], v[84:87], v[182:185], v[2:17]
	v_subrev_u32_e32 v168, 64, v168
	v_mfma_f32_32x32x16_bf16 v[2:17], v[66:69], v[186:189], v[2:17]
	v_mfma_f32_32x32x16_bf16 v[2:17], v[70:73], v[190:193], v[2:17]
	v_mov_b32_e32 v174, v79
	v_mov_b64_e32 v[66:67], v[222:223]
	v_mov_b64_e32 v[68:69], v[224:225]
	v_mov_b64_e32 v[70:71], v[226:227]
	v_mov_b64_e32 v[72:73], v[228:229]
	v_mov_b64_e32 v[74:75], v[230:231]
	v_mov_b64_e32 v[76:77], v[232:233]
	v_mov_b64_e32 v[78:79], v[234:235]
	v_mov_b64_e32 v[80:81], v[236:237]
	v_mov_b64_e32 v[82:83], v[206:207]
	v_mov_b64_e32 v[84:85], v[208:209]
	v_mov_b64_e32 v[86:87], v[210:211]
	v_mov_b64_e32 v[88:89], v[212:213]
	v_mov_b64_e32 v[90:91], v[214:215]
	v_mov_b64_e32 v[92:93], v[216:217]
	v_mov_b64_e32 v[94:95], v[218:219]
	v_mov_b64_e32 v[96:97], v[220:221]
	s_mov_b32 s56, s87
	s_mov_b32 s87, s88
	s_mov_b32 s88, s89
	s_mov_b32 s89, s56
	s_mov_b32 s56, s94
	s_mov_b32 s94, s95
	s_mov_b32 s95, s96
	s_mov_b32 s96, s97
	s_mov_b32 s97, s56
	s_branch .LBB0_805

.Latt1_noresc_f:
	v_cvt_pk_bf16_f32 v178, v82, v175
	v_cvt_pk_bf16_f32 v179, v84, v85
	v_cvt_pk_bf16_f32 v180, v86, v87
	v_cvt_pk_bf16_f32 v181, v88, v176
	v_cvt_pk_bf16_f32 v84, v89, v90
	v_cvt_pk_bf16_f32 v85, v91, v92
	v_cvt_pk_bf16_f32 v86, v93, v94
	v_cvt_pk_bf16_f32 v87, v95, v96
	v_cvt_pk_bf16_f32 v66, v66, v67
	v_cvt_pk_bf16_f32 v67, v68, v69
	v_cvt_pk_bf16_f32 v68, v70, v71
	v_cvt_pk_bf16_f32 v69, v72, v83
	v_cvt_pk_bf16_f32 v70, v73, v74
	v_cvt_pk_bf16_f32 v71, v75, v76
	v_cvt_pk_bf16_f32 v72, v77, v78
	v_cvt_pk_bf16_f32 v73, v80, v81
	v_add_u32_e32 v78, s94, v172
	ds_read_b64_tr_b16 v[74:75], v78 offset:0
	ds_read_b64_tr_b16 v[76:77], v78 offset:0x800
	ds_read_b64_tr_b16 v[80:81], v78 offset:0x1000
	ds_read_b64_tr_b16 v[82:83], v78 offset:0x1800
	ds_read_b64_tr_b16 v[88:89], v78 offset:0x2000
	ds_read_b64_tr_b16 v[90:91], v78 offset:0x2800
	ds_read_b64_tr_b16 v[92:93], v78 offset:0x3000
	v_add_f32_e32 v79, v79, v177
	ds_read_b64_tr_b16 v[94:95], v78 offset:0x3800
	v_fmac_f32_e32 v79, v174, v97
	ds_read_b64_tr_b16 v[174:175], v78 offset:0x200
	ds_read_b64_tr_b16 v[176:177], v78 offset:0xa00
	ds_read_b64_tr_b16 v[182:183], v78 offset:0x1200
	ds_read_b64_tr_b16 v[184:185], v78 offset:0x1a00
	ds_read_b64_tr_b16 v[186:187], v78 offset:0x2200
	ds_read_b64_tr_b16 v[188:189], v78 offset:0x2a00
	ds_read_b64_tr_b16 v[190:191], v78 offset:0x3200
	ds_read_b64_tr_b16 v[192:193], v78 offset:0x3a00
	s_waitcnt lgkmcnt(8)
	v_permlane32_swap_b32_e32 v178, v180
	v_permlane32_swap_b32_e32 v179, v181
	v_permlane32_swap_b32_e32 v84, v86
	v_permlane32_swap_b32_e32 v85, v87
	v_permlane32_swap_b32_e32 v66, v68
	v_permlane32_swap_b32_e32 v67, v69
	v_permlane32_swap_b32_e32 v70, v72
	v_permlane32_swap_b32_e32 v71, v73
	v_mfma_f32_32x32x16_bf16 v[50:65], v[178:181], v[74:77], v[50:65]
	ds_read_b64_tr_b16 v[74:75], v78 offset:0x400
	ds_read_b64_tr_b16 v[76:77], v78 offset:0xc00
	v_mfma_f32_32x32x16_bf16 v[50:65], v[84:87], v[80:83], v[50:65]
	ds_read_b64_tr_b16 v[80:81], v78 offset:0x1400
	ds_read_b64_tr_b16 v[82:83], v78 offset:0x1c00
	v_mfma_f32_32x32x16_bf16 v[50:65], v[66:69], v[88:91], v[50:65]
	ds_read_b64_tr_b16 v[88:89], v78 offset:0x2400
	ds_read_b64_tr_b16 v[90:91], v78 offset:0x2c00
	v_mfma_f32_32x32x16_bf16 v[50:65], v[70:73], v[92:95], v[50:65]
	ds_read_b64_tr_b16 v[92:93], v78 offset:0x3400
	ds_read_b64_tr_b16 v[94:95], v78 offset:0x3c00
	s_waitcnt lgkmcnt(8)
	v_mfma_f32_32x32x16_bf16 v[34:49], v[178:181], v[174:177], v[34:49]
	ds_read_b64_tr_b16 v[174:175], v78 offset:0x600
	ds_read_b64_tr_b16 v[176:177], v78 offset:0xe00
	v_mfma_f32_32x32x16_bf16 v[34:49], v[84:87], v[182:185], v[34:49]
	ds_read_b64_tr_b16 v[182:183], v78 offset:0x1600
	ds_read_b64_tr_b16 v[184:185], v78 offset:0x1e00
	v_mfma_f32_32x32x16_bf16 v[34:49], v[66:69], v[186:189], v[34:49]
	ds_read_b64_tr_b16 v[186:187], v78 offset:0x2600
	ds_read_b64_tr_b16 v[188:189], v78 offset:0x2e00
	v_mfma_f32_32x32x16_bf16 v[34:49], v[70:73], v[190:193], v[34:49]
	ds_read_b64_tr_b16 v[190:191], v78 offset:0x3600
	ds_read_b64_tr_b16 v[192:193], v78 offset:0x3e00
	s_waitcnt lgkmcnt(8)
	v_mfma_f32_32x32x16_bf16 v[18:33], v[178:181], v[74:77], v[18:33]
	s_waitcnt lgkmcnt(0)
	v_mfma_f32_32x32x16_bf16 v[18:33], v[84:87], v[80:83], v[18:33]
	v_mfma_f32_32x32x16_bf16 v[18:33], v[66:69], v[88:91], v[18:33]
	v_mfma_f32_32x32x16_bf16 v[18:33], v[70:73], v[92:95], v[18:33]
	v_mfma_f32_32x32x16_bf16 v[2:17], v[178:181], v[174:177], v[2:17]
	s_add_i32 s86, s86, 64
	s_add_i32 s12, s12, 1
	v_lshl_add_u64 v[150:151], v[150:151], 0, s[14:15]
	v_lshl_add_u64 v[152:153], v[152:153], 0, s[14:15]
	v_lshl_add_u64 v[154:155], v[154:155], 0, s[16:17]
	v_lshl_add_u64 v[156:157], v[156:157], 0, s[16:17]
	v_lshl_add_u64 v[158:159], v[158:159], 0, s[16:17]
	v_mfma_f32_32x32x16_bf16 v[2:17], v[84:87], v[182:185], v[2:17]
	v_subrev_u32_e32 v168, 64, v168
	v_mfma_f32_32x32x16_bf16 v[2:17], v[66:69], v[186:189], v[2:17]
	v_mfma_f32_32x32x16_bf16 v[2:17], v[70:73], v[190:193], v[2:17]
	s_branch .LBB0_815
